# strategy 7.11: dense attention main loop back edge rotated (counter/exit test/loop-carried moves in front of the loop-back barrier; exit path has its own barrier copy)
# speedup vs baseline: 1.0004x; 1.0004x over previous
.LBB0_736:
	s_waitcnt lgkmcnt(14)
	v_mfma_f32_32x32x16_bf16 v[16:31], v[144:147], v[152:155], v[16:31]
	v_exp_f32_e32 v98, v98
	v_exp_f32_e32 v99, v99
	v_exp_f32_e32 v100, v100
	v_exp_f32_e32 v101, v101
	s_waitcnt lgkmcnt(12)
	v_mfma_f32_32x32x16_bf16 v[0:15], v[144:147], v[148:151], v[0:15]
	v_exp_f32_e32 v102, v102
	v_exp_f32_e32 v103, v103
	v_exp_f32_e32 v104, v104
	v_exp_f32_e32 v105, v105
	v_add_u32_e32 v44, s13, v65
	ds_read_b128 v[176:179], v44
	ds_read_b128 v[172:175], v44 offset:512
	s_waitcnt lgkmcnt(12)
	v_mfma_f32_32x32x16_bf16 v[16:31], v[136:139], v[48:51], v[16:31]
	v_exp_f32_e32 v106, v106
	v_exp_f32_e32 v107, v107
	v_exp_f32_e32 v108, v108
	v_exp_f32_e32 v109, v109
	ds_read_b128 v[168:171], v44 offset:2048
	ds_read_b128 v[164:167], v44 offset:2560
	s_waitcnt lgkmcnt(12)
	v_mfma_f32_32x32x16_bf16 v[0:15], v[136:139], v[52:55], v[0:15]
	v_exp_f32_e32 v110, v110
	v_exp_f32_e32 v111, v111
	v_exp_f32_e32 v112, v112
	v_exp_f32_e32 v113, v113
	ds_read_b128 v[160:163], v44 offset:4096
	ds_read_b128 v[156:159], v44 offset:4608
	s_waitcnt lgkmcnt(12)
	v_mfma_f32_32x32x16_bf16 v[16:31], v[128:131], v[56:59], v[16:31]
	v_exp_f32_e32 v82, v82
	v_exp_f32_e32 v83, v83
	v_exp_f32_e32 v84, v84
	v_exp_f32_e32 v85, v85
	ds_read_b128 v[152:155], v44 offset:6144
	ds_read_b128 v[148:151], v44 offset:6656
	s_waitcnt lgkmcnt(12)
	v_mfma_f32_32x32x16_bf16 v[0:15], v[128:131], v[32:35], v[0:15]
	v_exp_f32_e32 v86, v86
	v_exp_f32_e32 v87, v87
	v_exp_f32_e32 v88, v88
	v_exp_f32_e32 v89, v89
	s_waitcnt lgkmcnt(10)
	v_mfma_f32_32x32x16_bf16 v[16:31], v[124:127], v[36:39], v[16:31]
	v_exp_f32_e32 v90, v90
	v_exp_f32_e32 v91, v91
	v_exp_f32_e32 v92, v92
	v_exp_f32_e32 v93, v93
	s_waitcnt lgkmcnt(8)
	v_mfma_f32_32x32x16_bf16 v[0:15], v[124:127], v[40:43], v[0:15]
	v_exp_f32_e32 v94, v94
	v_exp_f32_e32 v95, v95
	v_exp_f32_e32 v96, v96
	v_exp_f32_e32 v97, v97
	s_andn2_b64 vcc, exec, s[2:3]
	s_add_i32 s100, s13, 0x2000
	s_cmpk_lg_i32 s13, 0x4000
	s_cselect_b32 s15, s100, 0
	s_add_i32 s100, s24, 2
	s_mov_b64 s[22:23], 0x90000
	v_lshl_add_u64 v[184:185], v[184:185], 0, s[22:23]
	v_lshl_add_u64 v[186:187], v[186:187], 0, s[22:23]
	s_cmp_ge_u32 s100, s11
	s_cbranch_scc1 .Lattn_exit_bar
	s_mov_b32 s24, s100
	s_mov_b32 s2, s14
	s_mov_b32 s25, s13
	s_mov_b32 s14, s15
	s_waitcnt vmcnt(2) lgkmcnt(0)
	s_barrier
	s_cbranch_vccnz .LBB0_732
	s_waitcnt lgkmcnt(0)
	v_add_u32_e32 v44, s33, v247
	ds_read_b128 v[32:35], v44 offset:49248
	ds_read_b128 v[36:39], v44 offset:49216
	ds_read_b128 v[40:43], v44 offset:49152
	ds_read_b128 v[44:47], v44 offset:49184
	s_waitcnt lgkmcnt(3)
	v_pk_mul_f32 v[30:31], v[30:31], v[34:35]
	v_pk_mul_f32 v[28:29], v[28:29], v[32:33]
	s_waitcnt lgkmcnt(2)
	v_pk_mul_f32 v[26:27], v[26:27], v[38:39]
	v_pk_mul_f32 v[24:25], v[24:25], v[36:37]
	s_waitcnt lgkmcnt(0)
	v_pk_mul_f32 v[22:23], v[22:23], v[46:47]
	v_pk_mul_f32 v[20:21], v[20:21], v[44:45]
	v_pk_mul_f32 v[18:19], v[18:19], v[42:43]
	v_pk_mul_f32 v[16:17], v[16:17], v[40:41]
	v_pk_mul_f32 v[14:15], v[14:15], v[34:35]
	v_pk_mul_f32 v[12:13], v[12:13], v[32:33]
	v_pk_mul_f32 v[10:11], v[10:11], v[38:39]
	v_pk_mul_f32 v[8:9], v[8:9], v[36:37]
	v_pk_mul_f32 v[6:7], v[6:7], v[46:47]
	v_pk_mul_f32 v[4:5], v[4:5], v[44:45]
	v_pk_mul_f32 v[2:3], v[2:3], v[42:43]
	v_pk_mul_f32 v[0:1], v[0:1], v[40:41]
	s_branch .LBB0_732
.Lattn_exit_bar:
	s_waitcnt vmcnt(2) lgkmcnt(0)
	s_barrier
	s_cbranch_vccnz .LBB0_748
	s_waitcnt lgkmcnt(0)
	v_add_u32_e32 v44, s33, v247
	ds_read_b128 v[32:35], v44 offset:49248
	ds_read_b128 v[36:39], v44 offset:49216
	ds_read_b128 v[40:43], v44 offset:49152
	ds_read_b128 v[44:47], v44 offset:49184
	s_waitcnt lgkmcnt(3)
	v_pk_mul_f32 v[30:31], v[30:31], v[34:35]
	v_pk_mul_f32 v[28:29], v[28:29], v[32:33]
	s_waitcnt lgkmcnt(2)
	v_pk_mul_f32 v[26:27], v[26:27], v[38:39]
	v_pk_mul_f32 v[24:25], v[24:25], v[36:37]
	s_waitcnt lgkmcnt(0)
	v_pk_mul_f32 v[22:23], v[22:23], v[46:47]
	v_pk_mul_f32 v[20:21], v[20:21], v[44:45]
	v_pk_mul_f32 v[18:19], v[18:19], v[42:43]
	v_pk_mul_f32 v[16:17], v[16:17], v[40:41]
	v_pk_mul_f32 v[14:15], v[14:15], v[34:35]
	v_pk_mul_f32 v[12:13], v[12:13], v[32:33]
	v_pk_mul_f32 v[10:11], v[10:11], v[38:39]
	v_pk_mul_f32 v[8:9], v[8:9], v[36:37]
	v_pk_mul_f32 v[6:7], v[6:7], v[46:47]
	v_pk_mul_f32 v[4:5], v[4:5], v[44:45]
	v_pk_mul_f32 v[2:3], v[2:3], v[42:43]
	v_pk_mul_f32 v[0:1], v[0:1], v[40:41]
	s_branch .LBB0_748
